# v39 shifted by 16 bytes (four s_nop at the entry): code placement scan
# speedup vs baseline: 1.0007x; 1.0007x over previous
_Z10hybrid_fwd4Args:
	s_nop 0
	s_nop 0
	s_nop 0
	s_nop 0
	s_mov_b32 s99, 0
	s_load_dwordx2 s[78:79], s[0:1], 0xb0
	s_load_dwordx4 s[4:7], s[0:1], 0xa0
	s_mov_b32 s74, s2
	s_add_u32 s2, s0, 0xc0
	s_addc_u32 s3, s1, 0
	v_readfirstlane_b32 s64, v0
	s_waitcnt lgkmcnt(0)
	v_writelane_b32 v254, s4, 0
	s_mov_b32 s71, s74
	s_nop 0
	v_writelane_b32 v254, s5, 1
	v_writelane_b32 v254, s6, 2
	v_writelane_b32 v254, s7, 3
	s_load_dword s80, s[0:1], 0xc0
	s_load_dwordx8 s[4:11], s[0:1], 0x80
	s_waitcnt lgkmcnt(0)
	v_writelane_b32 v254, s4, 4
	s_nop 1
	v_writelane_b32 v254, s5, 5
	v_writelane_b32 v254, s6, 6
	v_writelane_b32 v254, s7, 7
	v_writelane_b32 v254, s8, 8
	v_writelane_b32 v254, s9, 9
	v_writelane_b32 v254, s10, 10
	v_writelane_b32 v254, s11, 11
	v_writelane_b32 v254, s2, 12
	s_nop 1
	v_writelane_b32 v254, s3, 13
	s_and_b32 s2, s80, 7
	s_cmp_lg_u32 s2, 0
	s_cbranch_scc0 .LBB0_42
	s_load_dwordx2 s[96:97], s[0:1], 0xb8
	v_cmp_gt_u32_e32 vcc, 4, v0
	s_and_saveexec_b64 s[4:5], vcc
